# plus write-through (sc1) stores for the input/output projection GEMM epilogues (P2, P6)
# baseline (speedup 1.0000x reference)
.LBB0_352:
	v_mov_b32_e32 v16, v188
	v_mov_b32_e32 v17, v189
	s_lshl_b32 s4, s54, 8
	s_nop 15
	s_nop 15
	s_add_i32 s4, s4, s73
	v_lshlrev_b32_e32 v18, 4, v16
	v_add_u32_e32 v28, s4, v17
	v_add_u32_e32 v19, v18, v17
	v_and_b32_e32 v33, 3, v17
	v_mul_lo_u32 v17, v17, s78
	v_ashrrev_i32_e32 v19, 2, v19
	v_add_u32_e32 v17, s76, v17
	v_add_u32_e32 v32, v17, v18
	v_mul_lo_u32 v17, v19, s78
	v_add_u32_e32 v17, s76, v17
	v_lshlrev_b32_e32 v178, 4, v33
	v_lshlrev_b32_e32 v26, 3, v16
	v_add_u32_e32 v30, s4, v19
	v_add_u32_e32 v25, v17, v178
	v_cmp_gt_i32_e32 vcc, 2, v16
	v_pk_mul_f32 v[18:19], v[146:147], s[34:35] op_sel_hi:[1,0]
	v_pk_mul_f32 v[16:17], v[144:145], s[34:35] op_sel_hi:[1,0]
	v_pk_mul_f32 v[20:21], v[150:151], s[34:35] op_sel_hi:[1,0]
	v_pk_mul_f32 v[22:23], v[148:149], s[34:35] op_sel_hi:[1,0]
	v_cvt_pk_bf16_f32 v16, v16, v17
	v_cvt_pk_bf16_f32 v17, v18, v19
	v_cvt_pk_bf16_f32 v18, v22, v23
	v_cvt_pk_bf16_f32 v19, v20, v21
	ds_write_b128 v32, v[16:19]
	v_pk_mul_f32 v[18:19], v[162:163], s[34:35] op_sel_hi:[1,0]
	v_pk_mul_f32 v[16:17], v[160:161], s[34:35] op_sel_hi:[1,0]
	v_pk_mul_f32 v[22:23], v[166:167], s[34:35] op_sel_hi:[1,0]
	v_pk_mul_f32 v[20:21], v[164:165], s[34:35] op_sel_hi:[1,0]
	v_cvt_pk_bf16_f32 v34, v16, v17
	v_cvt_pk_bf16_f32 v35, v18, v19
	v_cvt_pk_bf16_f32 v36, v20, v21
	v_cvt_pk_bf16_f32 v37, v22, v23
	v_ashrrev_i32_e32 v31, 31, v30
	s_lshl_b32 s4, s52, 8
	ds_write_b128 v32, v[34:37] offset:64
	v_lshlrev_b64 v[34:35], 13, v[30:31]
	s_ashr_i32 s5, s4, 31
	v_lshl_add_u64 v[42:43], s[14:15], 0, v[34:35]
	ds_read_b128 v[34:37], v25
	ds_read_b128 v[38:41], v25 offset:64
	s_cmp_eq_u32 s52, 15
	s_cselect_b64 s[6:7], -1, 0
	v_lshl_add_u64 v[42:43], s[4:5], 1, v[42:43]
	s_and_b64 s[6:7], s[30:31], s[6:7]
	v_lshl_add_u64 v[42:43], v[42:43], 0, s[12:13]
	s_and_b64 s[6:7], s[6:7], vcc
	v_ashrrev_i32_e32 v27, 31, v26
	v_lshl_add_u64 v[42:43], v[42:43], 0, v[178:179]
	v_ashrrev_i32_e32 v29, 31, v28
	s_waitcnt lgkmcnt(0)
	global_store_dwordx4 v[42:43], v[34:37], off sc1
	global_store_dwordx4 v[42:43], v[38:41], off offset:256 sc1
	s_and_saveexec_b64 s[28:29], s[6:7]
	s_cbranch_execz .LBB0_354
	v_lshlrev_b64 v[34:35], 6, v[28:29]
	v_lshl_add_u64 v[34:35], s[18:19], 0, v[34:35]
	v_lshl_add_u64 v[34:35], v[26:27], 2, v[34:35]
	global_store_dwordx4 v[34:35], v[16:19], off sc1
	global_store_dwordx4 v[34:35], v[20:23], off offset:16 sc1
.LBB0_354:
	s_or_b64 exec, exec, s[28:29]
	v_pk_mul_f32 v[18:19], v[122:123], s[34:35] op_sel_hi:[1,0]
	v_pk_mul_f32 v[16:17], v[120:121], s[34:35] op_sel_hi:[1,0]
	v_pk_mul_f32 v[20:21], v[126:127], s[34:35] op_sel_hi:[1,0]
	v_pk_mul_f32 v[22:23], v[124:125], s[34:35] op_sel_hi:[1,0]
	v_cvt_pk_bf16_f32 v16, v16, v17
	v_cvt_pk_bf16_f32 v17, v18, v19
	v_cvt_pk_bf16_f32 v18, v22, v23
	v_cvt_pk_bf16_f32 v19, v20, v21
	ds_write_b128 v32, v[16:19]
	v_pk_mul_f32 v[18:19], v[154:155], s[34:35] op_sel_hi:[1,0]
	v_pk_mul_f32 v[16:17], v[152:153], s[34:35] op_sel_hi:[1,0]
	v_pk_mul_f32 v[22:23], v[158:159], s[34:35] op_sel_hi:[1,0]
	v_pk_mul_f32 v[20:21], v[156:157], s[34:35] op_sel_hi:[1,0]
	v_cvt_pk_bf16_f32 v34, v16, v17
	v_cvt_pk_bf16_f32 v35, v18, v19
	v_cvt_pk_bf16_f32 v36, v20, v21
	v_cvt_pk_bf16_f32 v37, v22, v23
	ds_write_b128 v32, v[34:37] offset:64
	v_add_u32_e32 v34, 16, v30
	v_ashrrev_i32_e32 v35, 31, v34
	v_lshlrev_b64 v[34:35], 13, v[34:35]
	v_lshl_add_u64 v[34:35], s[14:15], 0, v[34:35]
	v_lshl_add_u64 v[42:43], s[4:5], 1, v[34:35]
	ds_read_b128 v[34:37], v25
	ds_read_b128 v[38:41], v25 offset:64
	v_lshlrev_b32_e32 v31, 3, v33
	v_lshl_add_u64 v[42:43], v[42:43], 0, s[12:13]
	v_lshlrev_b32_e32 v178, 1, v31
	v_lshl_add_u64 v[42:43], v[42:43], 0, v[178:179]
	s_waitcnt lgkmcnt(0)
	global_store_dwordx4 v[42:43], v[34:37], off sc1
	global_store_dwordx4 v[42:43], v[38:41], off offset:256 sc1
	s_and_saveexec_b64 s[28:29], s[6:7]
	s_cbranch_execz .LBB0_356
	v_lshlrev_b64 v[34:35], 6, v[28:29]
	v_lshl_add_u64 v[34:35], s[18:19], 0, v[34:35]
	v_lshl_add_u64 v[34:35], v[26:27], 2, v[34:35]
	global_store_dwordx4 v[34:35], v[16:19], off offset:1024 sc1
	global_store_dwordx4 v[34:35], v[20:23], off offset:1040 sc1
.LBB0_356:
	s_or_b64 exec, exec, s[28:29]
	v_pk_mul_f32 v[18:19], v[114:115], s[34:35] op_sel_hi:[1,0]
	v_pk_mul_f32 v[16:17], v[112:113], s[34:35] op_sel_hi:[1,0]
	v_pk_mul_f32 v[20:21], v[118:119], s[34:35] op_sel_hi:[1,0]
	v_pk_mul_f32 v[22:23], v[116:117], s[34:35] op_sel_hi:[1,0]
	v_cvt_pk_bf16_f32 v16, v16, v17
	v_cvt_pk_bf16_f32 v17, v18, v19
	v_cvt_pk_bf16_f32 v18, v22, v23
	v_cvt_pk_bf16_f32 v19, v20, v21
	ds_write_b128 v32, v[16:19]
	v_pk_mul_f32 v[18:19], v[130:131], s[34:35] op_sel_hi:[1,0]
	v_pk_mul_f32 v[16:17], v[128:129], s[34:35] op_sel_hi:[1,0]
	v_pk_mul_f32 v[22:23], v[134:135], s[34:35] op_sel_hi:[1,0]
	v_pk_mul_f32 v[20:21], v[132:133], s[34:35] op_sel_hi:[1,0]
	v_cvt_pk_bf16_f32 v34, v16, v17
	v_cvt_pk_bf16_f32 v35, v18, v19
	v_cvt_pk_bf16_f32 v36, v20, v21
	v_cvt_pk_bf16_f32 v37, v22, v23
	ds_write_b128 v32, v[34:37] offset:64
	v_add_u32_e32 v34, 32, v30
	v_ashrrev_i32_e32 v35, 31, v34
	v_lshlrev_b64 v[34:35], 13, v[34:35]
	v_lshl_add_u64 v[42:43], s[14:15], 0, v[34:35]
	ds_read_b128 v[34:37], v25
	ds_read_b128 v[38:41], v25 offset:64
	v_lshl_add_u64 v[42:43], s[4:5], 1, v[42:43]
	v_lshl_add_u64 v[42:43], v[42:43], 0, s[12:13]
	v_lshl_add_u64 v[42:43], v[42:43], 0, v[178:179]
	s_waitcnt lgkmcnt(0)
	global_store_dwordx4 v[42:43], v[34:37], off sc1
	global_store_dwordx4 v[42:43], v[38:41], off offset:256 sc1
	s_and_saveexec_b64 s[28:29], s[6:7]
	s_cbranch_execz .LBB0_358
	v_lshlrev_b64 v[34:35], 6, v[28:29]
	v_lshl_add_u64 v[34:35], s[18:19], 0, v[34:35]
	v_lshl_add_u64 v[34:35], v[26:27], 2, v[34:35]
	global_store_dwordx4 v[34:35], v[16:19], off offset:2048 sc1
	global_store_dwordx4 v[34:35], v[20:23], off offset:2064 sc1
.LBB0_358:
	s_or_b64 exec, exec, s[28:29]
	v_pk_mul_f32 v[18:19], v[90:91], s[34:35] op_sel_hi:[1,0]
	v_pk_mul_f32 v[16:17], v[88:89], s[34:35] op_sel_hi:[1,0]
	v_pk_mul_f32 v[20:21], v[94:95], s[34:35] op_sel_hi:[1,0]
	v_pk_mul_f32 v[22:23], v[92:93], s[34:35] op_sel_hi:[1,0]
	v_cvt_pk_bf16_f32 v16, v16, v17
	v_cvt_pk_bf16_f32 v17, v18, v19
	v_cvt_pk_bf16_f32 v18, v22, v23
	v_cvt_pk_bf16_f32 v19, v20, v21
	ds_write_b128 v32, v[16:19]
	v_pk_mul_f32 v[18:19], v[106:107], s[34:35] op_sel_hi:[1,0]
	v_pk_mul_f32 v[16:17], v[104:105], s[34:35] op_sel_hi:[1,0]
	v_pk_mul_f32 v[22:23], v[110:111], s[34:35] op_sel_hi:[1,0]
	v_pk_mul_f32 v[20:21], v[108:109], s[34:35] op_sel_hi:[1,0]
	v_cvt_pk_bf16_f32 v34, v16, v17
	v_cvt_pk_bf16_f32 v35, v18, v19
	v_cvt_pk_bf16_f32 v36, v20, v21
	v_cvt_pk_bf16_f32 v37, v22, v23
	ds_write_b128 v32, v[34:37] offset:64
	v_add_u32_e32 v34, 48, v30
	v_ashrrev_i32_e32 v35, 31, v34
	v_lshlrev_b64 v[34:35], 13, v[34:35]
	v_lshl_add_u64 v[42:43], s[14:15], 0, v[34:35]
	ds_read_b128 v[34:37], v25
	ds_read_b128 v[38:41], v25 offset:64
	v_lshl_add_u64 v[42:43], s[4:5], 1, v[42:43]
	v_lshl_add_u64 v[42:43], v[42:43], 0, s[12:13]
	v_lshl_add_u64 v[42:43], v[42:43], 0, v[178:179]
	s_waitcnt lgkmcnt(0)
	global_store_dwordx4 v[42:43], v[34:37], off sc1
	global_store_dwordx4 v[42:43], v[38:41], off offset:256 sc1
	s_and_saveexec_b64 s[28:29], s[6:7]
	s_cbranch_execz .LBB0_360
	v_lshlrev_b64 v[34:35], 6, v[28:29]
	v_lshl_add_u64 v[34:35], s[18:19], 0, v[34:35]
	v_lshl_add_u64 v[34:35], v[26:27], 2, v[34:35]
	global_store_dwordx4 v[34:35], v[16:19], off offset:3072 sc1
	global_store_dwordx4 v[34:35], v[20:23], off offset:3088 sc1
.LBB0_360:
	s_or_b64 exec, exec, s[28:29]
	v_pk_mul_f32 v[18:19], v[98:99], s[34:35] op_sel_hi:[1,0]
	v_pk_mul_f32 v[16:17], v[96:97], s[34:35] op_sel_hi:[1,0]
	v_pk_mul_f32 v[20:21], v[102:103], s[34:35] op_sel_hi:[1,0]
	v_pk_mul_f32 v[22:23], v[100:101], s[34:35] op_sel_hi:[1,0]
	v_cvt_pk_bf16_f32 v16, v16, v17
	v_cvt_pk_bf16_f32 v17, v18, v19
	v_cvt_pk_bf16_f32 v18, v22, v23
	v_cvt_pk_bf16_f32 v19, v20, v21
	v_add_u32_e32 v38, 0x80, v30
	ds_write_b128 v32, v[16:19]
	v_pk_mul_f32 v[18:19], v[138:139], s[34:35] op_sel_hi:[1,0]
	v_pk_mul_f32 v[16:17], v[136:137], s[34:35] op_sel_hi:[1,0]
	v_pk_mul_f32 v[22:23], v[142:143], s[34:35] op_sel_hi:[1,0]
	v_pk_mul_f32 v[20:21], v[140:141], s[34:35] op_sel_hi:[1,0]
	v_cvt_pk_bf16_f32 v34, v16, v17
	v_cvt_pk_bf16_f32 v35, v18, v19
	v_cvt_pk_bf16_f32 v36, v20, v21
	v_cvt_pk_bf16_f32 v37, v22, v23
	v_ashrrev_i32_e32 v39, 31, v38
	ds_write_b128 v32, v[34:37] offset:64
	v_lshlrev_b64 v[34:35], 13, v[38:39]
	v_lshl_add_u64 v[42:43], s[14:15], 0, v[34:35]
	ds_read_b128 v[34:37], v25
	ds_read_b128 v[38:41], v25 offset:64
	v_lshl_add_u64 v[42:43], s[4:5], 1, v[42:43]
	v_lshl_add_u64 v[42:43], v[42:43], 0, s[12:13]
	v_lshl_add_u64 v[42:43], v[42:43], 0, v[178:179]
	s_waitcnt lgkmcnt(0)
	global_store_dwordx4 v[42:43], v[34:37], off sc1
	global_store_dwordx4 v[42:43], v[38:41], off offset:256 sc1
	s_and_saveexec_b64 s[28:29], s[6:7]
	s_cbranch_execz .LBB0_362
	v_lshlrev_b64 v[34:35], 6, v[28:29]
	v_lshl_add_u64 v[34:35], s[18:19], 0, v[34:35]
	v_lshl_add_u64 v[34:35], v[26:27], 2, v[34:35]
	v_lshl_add_u64 v[36:37], v[34:35], 0, s[36:37]
	v_add_co_u32_e32 v34, vcc, 0x2000, v34
	s_nop 1
	v_addc_co_u32_e32 v35, vcc, 0, v35, vcc
	global_store_dwordx4 v[34:35], v[16:19], off sc1
	global_store_dwordx4 v[36:37], v[20:23], off offset:16 sc1
.LBB0_362:
	s_or_b64 exec, exec, s[28:29]
	v_pk_mul_f32 v[18:19], v[82:83], s[34:35] op_sel_hi:[1,0]
	v_pk_mul_f32 v[16:17], v[80:81], s[34:35] op_sel_hi:[1,0]
	v_pk_mul_f32 v[20:21], v[86:87], s[34:35] op_sel_hi:[1,0]
	v_pk_mul_f32 v[22:23], v[84:85], s[34:35] op_sel_hi:[1,0]
	v_cvt_pk_bf16_f32 v16, v16, v17
	v_cvt_pk_bf16_f32 v17, v18, v19
	v_cvt_pk_bf16_f32 v18, v22, v23
	v_cvt_pk_bf16_f32 v19, v20, v21
	ds_write_b128 v32, v[16:19]
	v_pk_mul_f32 v[18:19], v[58:59], s[34:35] op_sel_hi:[1,0]
	v_pk_mul_f32 v[16:17], v[56:57], s[34:35] op_sel_hi:[1,0]
	v_pk_mul_f32 v[22:23], v[62:63], s[34:35] op_sel_hi:[1,0]
	v_pk_mul_f32 v[20:21], v[60:61], s[34:35] op_sel_hi:[1,0]
	v_cvt_pk_bf16_f32 v34, v16, v17
	v_cvt_pk_bf16_f32 v35, v18, v19
	v_cvt_pk_bf16_f32 v36, v20, v21
	v_cvt_pk_bf16_f32 v37, v22, v23
	ds_write_b128 v32, v[34:37] offset:64
	v_add_u32_e32 v34, 0x90, v30
	v_ashrrev_i32_e32 v35, 31, v34
	v_lshlrev_b64 v[34:35], 13, v[34:35]
	v_lshl_add_u64 v[42:43], s[14:15], 0, v[34:35]
	ds_read_b128 v[34:37], v25
	ds_read_b128 v[38:41], v25 offset:64
	v_lshl_add_u64 v[42:43], s[4:5], 1, v[42:43]
	v_lshl_add_u64 v[42:43], v[42:43], 0, s[12:13]
	v_lshl_add_u64 v[42:43], v[42:43], 0, v[178:179]
	s_waitcnt lgkmcnt(0)
	global_store_dwordx4 v[42:43], v[34:37], off sc1
	global_store_dwordx4 v[42:43], v[38:41], off offset:256 sc1
	s_and_saveexec_b64 s[28:29], s[6:7]
	s_cbranch_execz .LBB0_364
	v_lshlrev_b64 v[34:35], 6, v[28:29]
	v_lshl_add_u64 v[34:35], s[18:19], 0, v[34:35]
	v_lshl_add_u64 v[34:35], v[26:27], 2, v[34:35]
	v_lshl_add_u64 v[36:37], v[34:35], 0, s[38:39]
	v_add_co_u32_e32 v34, vcc, 0x2000, v34
	s_nop 1
	v_addc_co_u32_e32 v35, vcc, 0, v35, vcc
	global_store_dwordx4 v[34:35], v[16:19], off offset:1024 sc1
	global_store_dwordx4 v[36:37], v[20:23], off offset:16 sc1
.LBB0_364:
	s_or_b64 exec, exec, s[28:29]
	v_pk_mul_f32 v[18:19], v[74:75], s[34:35] op_sel_hi:[1,0]
	v_pk_mul_f32 v[16:17], v[72:73], s[34:35] op_sel_hi:[1,0]
	v_pk_mul_f32 v[20:21], v[78:79], s[34:35] op_sel_hi:[1,0]
	v_pk_mul_f32 v[22:23], v[76:77], s[34:35] op_sel_hi:[1,0]
	v_cvt_pk_bf16_f32 v16, v16, v17
	v_cvt_pk_bf16_f32 v17, v18, v19
	v_cvt_pk_bf16_f32 v18, v22, v23
	v_cvt_pk_bf16_f32 v19, v20, v21
	v_pk_mul_f32 v[10:11], v[10:11], s[34:35] op_sel_hi:[1,0]
	v_pk_mul_f32 v[8:9], v[8:9], s[34:35] op_sel_hi:[1,0]
	v_pk_mul_f32 v[14:15], v[14:15], s[34:35] op_sel_hi:[1,0]
	v_pk_mul_f32 v[12:13], v[12:13], s[34:35] op_sel_hi:[1,0]
	ds_write_b128 v32, v[16:19]
	v_cvt_pk_bf16_f32 v16, v8, v9
	v_cvt_pk_bf16_f32 v17, v10, v11
	v_cvt_pk_bf16_f32 v18, v12, v13
	v_cvt_pk_bf16_f32 v19, v14, v15
	ds_write_b128 v32, v[16:19] offset:64
	v_add_u32_e32 v16, 0xa0, v30
	v_ashrrev_i32_e32 v17, 31, v16
	v_lshlrev_b64 v[16:17], 13, v[16:17]
	v_lshl_add_u64 v[34:35], s[14:15], 0, v[16:17]
	ds_read_b128 v[16:19], v25
	ds_read_b128 v[20:23], v25 offset:64
	v_lshl_add_u64 v[34:35], s[4:5], 1, v[34:35]
	v_lshl_add_u64 v[34:35], v[34:35], 0, s[12:13]
	v_lshl_add_u64 v[34:35], v[34:35], 0, v[178:179]
	s_waitcnt lgkmcnt(0)
	global_store_dwordx4 v[34:35], v[16:19], off sc1
	global_store_dwordx4 v[34:35], v[20:23], off offset:256 sc1
	s_and_saveexec_b64 s[28:29], s[6:7]
	s_cbranch_execz .LBB0_366
	v_lshlrev_b64 v[16:17], 6, v[28:29]
	v_lshl_add_u64 v[16:17], s[18:19], 0, v[16:17]
	v_lshl_add_u64 v[16:17], v[26:27], 2, v[16:17]
	v_lshl_add_u64 v[18:19], v[16:17], 0, s[40:41]
	v_add_co_u32_e32 v16, vcc, 0x2000, v16
	s_nop 1
	v_addc_co_u32_e32 v17, vcc, 0, v17, vcc
	global_store_dwordx4 v[16:17], v[8:11], off offset:2048 sc1
	global_store_dwordx4 v[18:19], v[12:15], off offset:16 sc1
.LBB0_366:
	s_or_b64 exec, exec, s[28:29]
	v_pk_mul_f32 v[10:11], v[70:71], s[34:35] op_sel_hi:[1,0]
	v_pk_mul_f32 v[8:9], v[68:69], s[34:35] op_sel_hi:[1,0]
	v_pk_mul_f32 v[12:13], v[66:67], s[34:35] op_sel_hi:[1,0]
	v_pk_mul_f32 v[14:15], v[64:65], s[34:35] op_sel_hi:[1,0]
	v_cvt_pk_bf16_f32 v8, v8, v9
	v_cvt_pk_bf16_f32 v9, v10, v11
	v_cvt_pk_bf16_f32 v10, v14, v15
	v_cvt_pk_bf16_f32 v11, v12, v13
	v_pk_mul_f32 v[6:7], v[6:7], s[34:35] op_sel_hi:[1,0]
	v_pk_mul_f32 v[4:5], v[4:5], s[34:35] op_sel_hi:[1,0]
	v_pk_mul_f32 v[2:3], v[2:3], s[34:35] op_sel_hi:[1,0]
	v_pk_mul_f32 v[0:1], v[0:1], s[34:35] op_sel_hi:[1,0]
	ds_write_b128 v32, v[8:11]
	v_cvt_pk_bf16_f32 v8, v4, v5
	v_cvt_pk_bf16_f32 v9, v6, v7
	v_cvt_pk_bf16_f32 v10, v0, v1
	v_cvt_pk_bf16_f32 v11, v2, v3
	ds_write_b128 v32, v[8:11] offset:64
	v_add_u32_e32 v8, 0xb0, v30
	v_ashrrev_i32_e32 v9, 31, v8
	v_lshlrev_b64 v[8:9], 13, v[8:9]
	v_lshl_add_u64 v[16:17], s[14:15], 0, v[8:9]
	ds_read_b128 v[8:11], v25
	ds_read_b128 v[12:15], v25 offset:64
	v_lshl_add_u64 v[16:17], s[4:5], 1, v[16:17]
	v_lshl_add_u64 v[16:17], v[16:17], 0, s[12:13]
	v_lshl_add_u64 v[16:17], v[16:17], 0, v[178:179]
	s_waitcnt lgkmcnt(0)
	global_store_dwordx4 v[16:17], v[8:11], off sc1
	global_store_dwordx4 v[16:17], v[12:15], off offset:256 sc1
	s_and_saveexec_b64 s[4:5], s[6:7]
	s_cbranch_execz .LBB0_332
	v_lshlrev_b64 v[8:9], 6, v[28:29]
	v_lshl_add_u64 v[8:9], s[18:19], 0, v[8:9]
	v_lshl_add_u64 v[8:9], v[26:27], 2, v[8:9]
	v_lshl_add_u64 v[10:11], v[8:9], 0, s[42:43]
	v_add_co_u32_e32 v8, vcc, 0x2000, v8
	s_nop 1
	v_addc_co_u32_e32 v9, vcc, 0, v9, vcc
	global_store_dwordx4 v[8:9], v[4:7], off offset:3072 sc1
	global_store_dwordx4 v[10:11], v[0:3], off offset:16 sc1
	s_branch .LBB0_332

.LBB0_1114:
	v_mov_b32_e32 v17, v190
	v_mov_b32_e32 v18, v189
	s_nop 15
	s_nop 15
	s_lshl_b32 s4, s44, 8
	v_lshlrev_b32_e32 v18, 4, v18
	v_mul_lo_u32 v20, v17, s67
	v_add_u32_e32 v19, v18, v17
	v_add3_u32 v30, s65, v20, v18
	v_pk_mul_f32 v[22:23], v[130:131], s[30:31] op_sel_hi:[1,0]
	v_pk_mul_f32 v[20:21], v[128:129], s[30:31] op_sel_hi:[1,0]
	v_pk_mul_f32 v[24:25], v[142:143], s[30:31] op_sel_hi:[1,0]
	v_pk_mul_f32 v[26:27], v[140:141], s[30:31] op_sel_hi:[1,0]
	s_add_i32 s4, s4, s63
	v_ashrrev_i32_e32 v19, 2, v19
	v_lshlrev_b32_e32 v17, 4, v17
	v_cvt_pk_bf16_f32 v20, v20, v21
	v_cvt_pk_bf16_f32 v21, v22, v23
	v_cvt_pk_bf16_f32 v22, v26, v27
	v_cvt_pk_bf16_f32 v23, v24, v25
	v_add_u32_e32 v18, s4, v19
	v_mul_lo_u32 v19, v19, s67
	v_and_b32_e32 v178, 48, v17
	ds_write_b128 v30, v[20:23]
	v_pk_mul_f32 v[22:23], v[162:163], s[30:31] op_sel_hi:[1,0]
	v_pk_mul_f32 v[20:21], v[160:161], s[30:31] op_sel_hi:[1,0]
	v_pk_mul_f32 v[24:25], v[166:167], s[30:31] op_sel_hi:[1,0]
	v_pk_mul_f32 v[26:27], v[164:165], s[30:31] op_sel_hi:[1,0]
	s_lshl_b32 s4, s35, 8
	v_add3_u32 v17, s65, v19, v178
	v_cvt_pk_bf16_f32 v20, v20, v21
	v_cvt_pk_bf16_f32 v21, v22, v23
	v_cvt_pk_bf16_f32 v22, v26, v27
	v_cvt_pk_bf16_f32 v23, v24, v25
	v_ashrrev_i32_e32 v19, 31, v18
	s_ashr_i32 s5, s4, 31
	ds_write_b128 v30, v[20:23] offset:64
	v_lshlrev_b64 v[20:21], 12, v[18:19]
	v_lshl_add_u64 v[20:21], s[18:19], 0, v[20:21]
	s_lshl_b64 s[4:5], s[4:5], 1
	v_lshl_add_u64 v[28:29], v[20:21], 0, s[4:5]
	ds_read_b128 v[20:23], v17
	ds_read_b128 v[24:27], v17 offset:64
	s_mov_b32 s35, s8
	v_lshl_add_u64 v[28:29], v[28:29], 0, s[34:35]
	v_lshl_add_u64 v[28:29], v[28:29], 0, v[178:179]
	s_waitcnt lgkmcnt(0)
	global_store_dwordx4 v[28:29], v[20:23], off sc1
	global_store_dwordx4 v[28:29], v[24:27], off offset:256 sc1
	s_nop 0
	v_pk_mul_f32 v[22:23], v[122:123], s[30:31] op_sel_hi:[1,0]
	v_pk_mul_f32 v[20:21], v[120:121], s[30:31] op_sel_hi:[1,0]
	v_pk_mul_f32 v[24:25], v[126:127], s[30:31] op_sel_hi:[1,0]
	v_pk_mul_f32 v[26:27], v[124:125], s[30:31] op_sel_hi:[1,0]
	v_cvt_pk_bf16_f32 v20, v20, v21
	v_cvt_pk_bf16_f32 v21, v22, v23
	v_cvt_pk_bf16_f32 v22, v26, v27
	v_cvt_pk_bf16_f32 v23, v24, v25
	ds_write_b128 v30, v[20:23]
	v_pk_mul_f32 v[22:23], v[146:147], s[30:31] op_sel_hi:[1,0]
	v_pk_mul_f32 v[20:21], v[144:145], s[30:31] op_sel_hi:[1,0]
	v_pk_mul_f32 v[24:25], v[150:151], s[30:31] op_sel_hi:[1,0]
	v_pk_mul_f32 v[26:27], v[148:149], s[30:31] op_sel_hi:[1,0]
	v_cvt_pk_bf16_f32 v20, v20, v21
	v_cvt_pk_bf16_f32 v21, v22, v23
	v_cvt_pk_bf16_f32 v22, v26, v27
	v_cvt_pk_bf16_f32 v23, v24, v25
	ds_write_b128 v30, v[20:23] offset:64
	v_add_u32_e32 v20, 16, v18
	v_ashrrev_i32_e32 v21, 31, v20
	v_lshlrev_b64 v[20:21], 12, v[20:21]
	v_lshl_add_u64 v[28:29], s[18:19], 0, v[20:21]
	ds_read_b128 v[20:23], v17
	ds_read_b128 v[24:27], v17 offset:64
	v_lshl_add_u64 v[28:29], v[28:29], 0, s[4:5]
	v_lshl_add_u64 v[28:29], v[28:29], 0, s[34:35]
	v_lshl_add_u64 v[28:29], v[28:29], 0, v[178:179]
	s_waitcnt lgkmcnt(0)
	global_store_dwordx4 v[28:29], v[20:23], off sc1
	global_store_dwordx4 v[28:29], v[24:27], off offset:256 sc1
	s_nop 0
	v_pk_mul_f32 v[22:23], v[98:99], s[30:31] op_sel_hi:[1,0]
	v_pk_mul_f32 v[20:21], v[96:97], s[30:31] op_sel_hi:[1,0]
	v_pk_mul_f32 v[24:25], v[102:103], s[30:31] op_sel_hi:[1,0]
	v_pk_mul_f32 v[26:27], v[100:101], s[30:31] op_sel_hi:[1,0]
	v_cvt_pk_bf16_f32 v20, v20, v21
	v_cvt_pk_bf16_f32 v21, v22, v23
	v_cvt_pk_bf16_f32 v22, v26, v27
	v_cvt_pk_bf16_f32 v23, v24, v25
	ds_write_b128 v30, v[20:23]
	v_pk_mul_f32 v[22:23], v[134:135], s[30:31] op_sel_hi:[1,0]
	v_pk_mul_f32 v[20:21], v[132:133], s[30:31] op_sel_hi:[1,0]
	v_pk_mul_f32 v[24:25], v[138:139], s[30:31] op_sel_hi:[1,0]
	v_pk_mul_f32 v[26:27], v[136:137], s[30:31] op_sel_hi:[1,0]
	v_cvt_pk_bf16_f32 v20, v20, v21
	v_cvt_pk_bf16_f32 v21, v22, v23
	v_cvt_pk_bf16_f32 v22, v26, v27
	v_cvt_pk_bf16_f32 v23, v24, v25
	ds_write_b128 v30, v[20:23] offset:64
	v_add_u32_e32 v20, 32, v18
	v_ashrrev_i32_e32 v21, 31, v20
	v_lshlrev_b64 v[20:21], 12, v[20:21]
	v_lshl_add_u64 v[28:29], s[18:19], 0, v[20:21]
	ds_read_b128 v[20:23], v17
	ds_read_b128 v[24:27], v17 offset:64
	v_lshl_add_u64 v[28:29], v[28:29], 0, s[4:5]
	v_lshl_add_u64 v[28:29], v[28:29], 0, s[34:35]
	v_lshl_add_u64 v[28:29], v[28:29], 0, v[178:179]
	s_waitcnt lgkmcnt(0)
	global_store_dwordx4 v[28:29], v[20:23], off sc1
	global_store_dwordx4 v[28:29], v[24:27], off offset:256 sc1
	s_nop 0
	v_pk_mul_f32 v[22:23], v[82:83], s[30:31] op_sel_hi:[1,0]
	v_pk_mul_f32 v[20:21], v[80:81], s[30:31] op_sel_hi:[1,0]
	v_pk_mul_f32 v[24:25], v[86:87], s[30:31] op_sel_hi:[1,0]
	v_pk_mul_f32 v[26:27], v[84:85], s[30:31] op_sel_hi:[1,0]
	v_cvt_pk_bf16_f32 v20, v20, v21
	v_cvt_pk_bf16_f32 v21, v22, v23
	v_cvt_pk_bf16_f32 v22, v26, v27
	v_cvt_pk_bf16_f32 v23, v24, v25
	ds_write_b128 v30, v[20:23]
	v_pk_mul_f32 v[22:23], v[106:107], s[30:31] op_sel_hi:[1,0]
	v_pk_mul_f32 v[20:21], v[104:105], s[30:31] op_sel_hi:[1,0]
	v_pk_mul_f32 v[24:25], v[110:111], s[30:31] op_sel_hi:[1,0]
	v_pk_mul_f32 v[26:27], v[108:109], s[30:31] op_sel_hi:[1,0]
	v_cvt_pk_bf16_f32 v20, v20, v21
	v_cvt_pk_bf16_f32 v21, v22, v23
	v_cvt_pk_bf16_f32 v22, v26, v27
	v_cvt_pk_bf16_f32 v23, v24, v25
	ds_write_b128 v30, v[20:23] offset:64
	v_add_u32_e32 v20, 48, v18
	v_ashrrev_i32_e32 v21, 31, v20
	v_lshlrev_b64 v[20:21], 12, v[20:21]
	v_lshl_add_u64 v[28:29], s[18:19], 0, v[20:21]
	ds_read_b128 v[20:23], v17
	ds_read_b128 v[24:27], v17 offset:64
	v_lshl_add_u64 v[28:29], v[28:29], 0, s[4:5]
	v_lshl_add_u64 v[28:29], v[28:29], 0, s[34:35]
	v_lshl_add_u64 v[28:29], v[28:29], 0, v[178:179]
	s_waitcnt lgkmcnt(0)
	global_store_dwordx4 v[28:29], v[20:23], off sc1
	global_store_dwordx4 v[28:29], v[24:27], off offset:256 sc1
	s_nop 0
	v_pk_mul_f32 v[22:23], v[114:115], s[30:31] op_sel_hi:[1,0]
	v_pk_mul_f32 v[20:21], v[112:113], s[30:31] op_sel_hi:[1,0]
	v_pk_mul_f32 v[26:27], v[118:119], s[30:31] op_sel_hi:[1,0]
	v_pk_mul_f32 v[28:29], v[116:117], s[30:31] op_sel_hi:[1,0]
	v_cvt_pk_bf16_f32 v20, v20, v21
	v_cvt_pk_bf16_f32 v21, v22, v23
	v_cvt_pk_bf16_f32 v22, v28, v29
	v_cvt_pk_bf16_f32 v23, v26, v27
	v_add_u32_e32 v24, 0x80, v18
	ds_write_b128 v30, v[20:23]
	v_pk_mul_f32 v[22:23], v[154:155], s[30:31] op_sel_hi:[1,0]
	v_pk_mul_f32 v[20:21], v[152:153], s[30:31] op_sel_hi:[1,0]
	v_pk_mul_f32 v[26:27], v[158:159], s[30:31] op_sel_hi:[1,0]
	v_pk_mul_f32 v[28:29], v[156:157], s[30:31] op_sel_hi:[1,0]
	v_cvt_pk_bf16_f32 v20, v20, v21
	v_cvt_pk_bf16_f32 v21, v22, v23
	v_cvt_pk_bf16_f32 v22, v28, v29
	v_cvt_pk_bf16_f32 v23, v26, v27
	v_ashrrev_i32_e32 v25, 31, v24
	ds_write_b128 v30, v[20:23] offset:64
	v_lshlrev_b64 v[20:21], 12, v[24:25]
	v_lshl_add_u64 v[28:29], s[18:19], 0, v[20:21]
	ds_read_b128 v[20:23], v17
	ds_read_b128 v[24:27], v17 offset:64
	v_lshl_add_u64 v[28:29], v[28:29], 0, s[4:5]
	v_lshl_add_u64 v[28:29], v[28:29], 0, s[34:35]
	v_lshl_add_u64 v[28:29], v[28:29], 0, v[178:179]
	s_waitcnt lgkmcnt(0)
	global_store_dwordx4 v[28:29], v[20:23], off sc1
	global_store_dwordx4 v[28:29], v[24:27], off offset:256 sc1
	s_nop 0
	v_pk_mul_f32 v[22:23], v[90:91], s[30:31] op_sel_hi:[1,0]
	v_pk_mul_f32 v[20:21], v[88:89], s[30:31] op_sel_hi:[1,0]
	v_pk_mul_f32 v[24:25], v[94:95], s[30:31] op_sel_hi:[1,0]
	v_pk_mul_f32 v[26:27], v[92:93], s[30:31] op_sel_hi:[1,0]
	v_cvt_pk_bf16_f32 v20, v20, v21
	v_cvt_pk_bf16_f32 v21, v22, v23
	v_cvt_pk_bf16_f32 v22, v26, v27
	v_cvt_pk_bf16_f32 v23, v24, v25
	ds_write_b128 v30, v[20:23]
	v_pk_mul_f32 v[22:23], v[58:59], s[30:31] op_sel_hi:[1,0]
	v_pk_mul_f32 v[20:21], v[56:57], s[30:31] op_sel_hi:[1,0]
	v_pk_mul_f32 v[24:25], v[62:63], s[30:31] op_sel_hi:[1,0]
	v_pk_mul_f32 v[26:27], v[60:61], s[30:31] op_sel_hi:[1,0]
	v_cvt_pk_bf16_f32 v20, v20, v21
	v_cvt_pk_bf16_f32 v21, v22, v23
	v_cvt_pk_bf16_f32 v22, v26, v27
	v_cvt_pk_bf16_f32 v23, v24, v25
	ds_write_b128 v30, v[20:23] offset:64
	v_add_u32_e32 v20, 0x90, v18
	v_ashrrev_i32_e32 v21, 31, v20
	v_lshlrev_b64 v[20:21], 12, v[20:21]
	v_lshl_add_u64 v[28:29], s[18:19], 0, v[20:21]
	ds_read_b128 v[20:23], v17
	ds_read_b128 v[24:27], v17 offset:64
	v_lshl_add_u64 v[28:29], v[28:29], 0, s[4:5]
	v_lshl_add_u64 v[28:29], v[28:29], 0, s[34:35]
	v_pk_mul_f32 v[10:11], v[10:11], s[30:31] op_sel_hi:[1,0]
	v_pk_mul_f32 v[8:9], v[8:9], s[30:31] op_sel_hi:[1,0]
	v_pk_mul_f32 v[14:15], v[14:15], s[30:31] op_sel_hi:[1,0]
	v_pk_mul_f32 v[12:13], v[12:13], s[30:31] op_sel_hi:[1,0]
	v_lshl_add_u64 v[28:29], v[28:29], 0, v[178:179]
	v_cvt_pk_bf16_f32 v8, v8, v9
	v_cvt_pk_bf16_f32 v9, v10, v11
	v_cvt_pk_bf16_f32 v10, v12, v13
	v_cvt_pk_bf16_f32 v11, v14, v15
	s_waitcnt lgkmcnt(0)
	global_store_dwordx4 v[28:29], v[20:23], off sc1
	global_store_dwordx4 v[28:29], v[24:27], off offset:256 sc1
	ds_write_b128 v30, v[8:11] offset:64
	v_pk_mul_f32 v[22:23], v[74:75], s[30:31] op_sel_hi:[1,0]
	v_pk_mul_f32 v[20:21], v[72:73], s[30:31] op_sel_hi:[1,0]
	v_pk_mul_f32 v[24:25], v[78:79], s[30:31] op_sel_hi:[1,0]
	v_pk_mul_f32 v[26:27], v[76:77], s[30:31] op_sel_hi:[1,0]
	v_add_u32_e32 v8, 0xa0, v18
	v_cvt_pk_bf16_f32 v20, v20, v21
	v_cvt_pk_bf16_f32 v21, v22, v23
	v_cvt_pk_bf16_f32 v22, v26, v27
	v_cvt_pk_bf16_f32 v23, v24, v25
	v_ashrrev_i32_e32 v9, 31, v8
	ds_write_b128 v30, v[20:23]
	v_lshlrev_b64 v[8:9], 12, v[8:9]
	v_lshl_add_u64 v[20:21], s[18:19], 0, v[8:9]
	ds_read_b128 v[8:11], v17
	ds_read_b128 v[12:15], v17 offset:64
	v_lshl_add_u64 v[20:21], v[20:21], 0, s[4:5]
	v_lshl_add_u64 v[20:21], v[20:21], 0, s[34:35]
	v_lshl_add_u64 v[20:21], v[20:21], 0, v[178:179]
	s_waitcnt lgkmcnt(0)
	global_store_dwordx4 v[20:21], v[8:11], off sc1
	global_store_dwordx4 v[20:21], v[12:15], off offset:256 sc1
	s_nop 0
	v_pk_mul_f32 v[10:11], v[70:71], s[30:31] op_sel_hi:[1,0]
	v_pk_mul_f32 v[8:9], v[68:69], s[30:31] op_sel_hi:[1,0]
	v_pk_mul_f32 v[12:13], v[66:67], s[30:31] op_sel_hi:[1,0]
	v_pk_mul_f32 v[14:15], v[64:65], s[30:31] op_sel_hi:[1,0]
	v_cvt_pk_bf16_f32 v8, v8, v9
	v_cvt_pk_bf16_f32 v9, v10, v11
	v_cvt_pk_bf16_f32 v10, v14, v15
	v_cvt_pk_bf16_f32 v11, v12, v13
	ds_write_b128 v30, v[8:11]
	v_pk_mul_f32 v[6:7], v[6:7], s[30:31] op_sel_hi:[1,0]
	v_pk_mul_f32 v[4:5], v[4:5], s[30:31] op_sel_hi:[1,0]
	v_pk_mul_f32 v[8:9], v[2:3], s[30:31] op_sel_hi:[1,0]
	v_pk_mul_f32 v[2:3], v[0:1], s[30:31] op_sel_hi:[1,0]
	v_cvt_pk_bf16_f32 v0, v4, v5
	v_cvt_pk_bf16_f32 v1, v6, v7
	v_cvt_pk_bf16_f32 v2, v2, v3
	v_cvt_pk_bf16_f32 v3, v8, v9
	ds_write_b128 v30, v[0:3] offset:64
	v_add_u32_e32 v0, 0xb0, v18
	v_ashrrev_i32_e32 v1, 31, v0
	v_lshlrev_b64 v[0:1], 12, v[0:1]
	v_lshl_add_u64 v[8:9], s[18:19], 0, v[0:1]
	ds_read_b128 v[0:3], v17
	ds_read_b128 v[4:7], v17 offset:64
	v_lshl_add_u64 v[8:9], v[8:9], 0, s[4:5]
	v_lshl_add_u64 v[8:9], v[8:9], 0, s[34:35]
	v_lshl_add_u64 v[8:9], v[8:9], 0, v[178:179]
	s_mov_b64 s[4:5], -1
	s_andn2_b64 vcc, exec, s[2:3]
	s_mov_b32 s35, s36
	s_mov_b32 s44, s38
	s_mov_b64 s[46:47], s[42:43]
	s_mov_b64 s[48:49], s[40:41]
	s_waitcnt lgkmcnt(0)
	global_store_dwordx4 v[8:9], v[0:3], off sc1
	global_store_dwordx4 v[8:9], v[4:7], off offset:256 sc1
	s_cbranch_vccz .LBB0_1133

.LBB0_1629:
	v_mov_b32_e32 v16, v189
	v_mov_b32_e32 v17, v188
	s_lshl_b32 s4, s54, 8
	s_nop 15
	s_nop 15
	s_add_i32 s4, s4, s73
	v_lshlrev_b32_e32 v18, 4, v17
	v_add_u32_e32 v28, s4, v16
	v_add_u32_e32 v19, v18, v16
	v_and_b32_e32 v33, 3, v16
	v_mul_lo_u32 v16, v16, s78
	v_ashrrev_i32_e32 v19, 2, v19
	v_add_u32_e32 v16, s76, v16
	v_add_u32_e32 v32, v16, v18
	v_mul_lo_u32 v16, v19, s78
	v_add_u32_e32 v16, s76, v16
	v_lshlrev_b32_e32 v178, 4, v33
	v_lshlrev_b32_e32 v26, 3, v17
	v_add_u32_e32 v30, s4, v19
	v_add_u32_e32 v25, v16, v178
	v_cmp_gt_i32_e32 vcc, 2, v17
	v_pk_mul_f32 v[18:19], v[146:147], s[34:35] op_sel_hi:[1,0]
	v_pk_mul_f32 v[16:17], v[144:145], s[34:35] op_sel_hi:[1,0]
	v_pk_mul_f32 v[20:21], v[150:151], s[34:35] op_sel_hi:[1,0]
	v_pk_mul_f32 v[22:23], v[148:149], s[34:35] op_sel_hi:[1,0]
	v_cvt_pk_bf16_f32 v16, v16, v17
	v_cvt_pk_bf16_f32 v17, v18, v19
	v_cvt_pk_bf16_f32 v18, v22, v23
	v_cvt_pk_bf16_f32 v19, v20, v21
	ds_write_b128 v32, v[16:19]
	v_pk_mul_f32 v[18:19], v[162:163], s[34:35] op_sel_hi:[1,0]
	v_pk_mul_f32 v[16:17], v[160:161], s[34:35] op_sel_hi:[1,0]
	v_pk_mul_f32 v[22:23], v[166:167], s[34:35] op_sel_hi:[1,0]
	v_pk_mul_f32 v[20:21], v[164:165], s[34:35] op_sel_hi:[1,0]
	v_cvt_pk_bf16_f32 v34, v16, v17
	v_cvt_pk_bf16_f32 v35, v18, v19
	v_cvt_pk_bf16_f32 v36, v20, v21
	v_cvt_pk_bf16_f32 v37, v22, v23
	v_ashrrev_i32_e32 v31, 31, v30
	s_lshl_b32 s4, s52, 8
	ds_write_b128 v32, v[34:37] offset:64
	v_lshlrev_b64 v[34:35], 13, v[30:31]
	s_ashr_i32 s5, s4, 31
	v_lshl_add_u64 v[42:43], s[14:15], 0, v[34:35]
	ds_read_b128 v[34:37], v25
	ds_read_b128 v[38:41], v25 offset:64
	s_cmp_eq_u32 s52, 15
	s_cselect_b64 s[6:7], -1, 0
	v_lshl_add_u64 v[42:43], s[4:5], 1, v[42:43]
	s_and_b64 s[6:7], s[30:31], s[6:7]
	v_lshl_add_u64 v[42:43], v[42:43], 0, s[12:13]
	s_and_b64 s[6:7], s[6:7], vcc
	v_ashrrev_i32_e32 v27, 31, v26
	v_lshl_add_u64 v[42:43], v[42:43], 0, v[178:179]
	v_ashrrev_i32_e32 v29, 31, v28
	s_waitcnt lgkmcnt(0)
	global_store_dwordx4 v[42:43], v[34:37], off sc1
	global_store_dwordx4 v[42:43], v[38:41], off offset:256 sc1
	s_and_saveexec_b64 s[28:29], s[6:7]
	s_cbranch_execz .LBB0_1631
	v_lshlrev_b64 v[34:35], 6, v[28:29]
	v_lshl_add_u64 v[34:35], s[18:19], 0, v[34:35]
	v_lshl_add_u64 v[34:35], v[26:27], 2, v[34:35]
	global_store_dwordx4 v[34:35], v[16:19], off sc1
	global_store_dwordx4 v[34:35], v[20:23], off offset:16 sc1

.LBB0_2391:
	v_mov_b32_e32 v17, v189
	v_mov_b32_e32 v19, v190
	s_nop 15
	s_nop 15
	s_lshl_b32 s4, s44, 8
	v_lshlrev_b32_e32 v17, 4, v17
	v_add_u32_e32 v18, v17, v19
	s_add_i32 s4, s4, s63
	v_ashrrev_i32_e32 v20, 2, v18
	v_mul_lo_u32 v18, v19, s67
	v_lshlrev_b32_e32 v19, 4, v19
	v_add3_u32 v17, s65, v18, v17
	v_add_u32_e32 v18, s4, v20
	v_mul_lo_u32 v20, v20, s67
	v_and_b32_e32 v178, 48, v19
	v_add3_u32 v30, s65, v20, v178
	v_pk_mul_f32 v[22:23], v[130:131], s[30:31] op_sel_hi:[1,0]
	v_pk_mul_f32 v[20:21], v[128:129], s[30:31] op_sel_hi:[1,0]
	v_pk_mul_f32 v[24:25], v[142:143], s[30:31] op_sel_hi:[1,0]
	v_pk_mul_f32 v[26:27], v[140:141], s[30:31] op_sel_hi:[1,0]
	v_cvt_pk_bf16_f32 v20, v20, v21
	v_cvt_pk_bf16_f32 v21, v22, v23
	v_cvt_pk_bf16_f32 v22, v26, v27
	v_cvt_pk_bf16_f32 v23, v24, v25
	ds_write_b128 v17, v[20:23]
	v_pk_mul_f32 v[22:23], v[162:163], s[30:31] op_sel_hi:[1,0]
	v_pk_mul_f32 v[20:21], v[160:161], s[30:31] op_sel_hi:[1,0]
	v_pk_mul_f32 v[24:25], v[166:167], s[30:31] op_sel_hi:[1,0]
	v_pk_mul_f32 v[26:27], v[164:165], s[30:31] op_sel_hi:[1,0]
	s_lshl_b32 s4, s35, 8
	v_cvt_pk_bf16_f32 v20, v20, v21
	v_cvt_pk_bf16_f32 v21, v22, v23
	v_cvt_pk_bf16_f32 v22, v26, v27
	v_cvt_pk_bf16_f32 v23, v24, v25
	v_ashrrev_i32_e32 v19, 31, v18
	s_ashr_i32 s5, s4, 31
	ds_write_b128 v17, v[20:23] offset:64
	v_lshlrev_b64 v[20:21], 12, v[18:19]
	v_lshl_add_u64 v[20:21], s[18:19], 0, v[20:21]
	s_lshl_b64 s[4:5], s[4:5], 1
	v_lshl_add_u64 v[28:29], v[20:21], 0, s[4:5]
	ds_read_b128 v[20:23], v30
	ds_read_b128 v[24:27], v30 offset:64
	s_mov_b32 s35, s8
	v_lshl_add_u64 v[28:29], v[28:29], 0, s[34:35]
	v_lshl_add_u64 v[28:29], v[28:29], 0, v[178:179]
	s_waitcnt lgkmcnt(0)
	global_store_dwordx4 v[28:29], v[20:23], off sc1
	global_store_dwordx4 v[28:29], v[24:27], off offset:256 sc1
	s_nop 0
	v_pk_mul_f32 v[22:23], v[122:123], s[30:31] op_sel_hi:[1,0]
	v_pk_mul_f32 v[20:21], v[120:121], s[30:31] op_sel_hi:[1,0]
	v_pk_mul_f32 v[24:25], v[126:127], s[30:31] op_sel_hi:[1,0]
	v_pk_mul_f32 v[26:27], v[124:125], s[30:31] op_sel_hi:[1,0]
	v_cvt_pk_bf16_f32 v20, v20, v21
	v_cvt_pk_bf16_f32 v21, v22, v23
	v_cvt_pk_bf16_f32 v22, v26, v27
	v_cvt_pk_bf16_f32 v23, v24, v25
	ds_write_b128 v17, v[20:23]
	v_pk_mul_f32 v[22:23], v[146:147], s[30:31] op_sel_hi:[1,0]
	v_pk_mul_f32 v[20:21], v[144:145], s[30:31] op_sel_hi:[1,0]
	v_pk_mul_f32 v[24:25], v[150:151], s[30:31] op_sel_hi:[1,0]
	v_pk_mul_f32 v[26:27], v[148:149], s[30:31] op_sel_hi:[1,0]
	v_cvt_pk_bf16_f32 v20, v20, v21
	v_cvt_pk_bf16_f32 v21, v22, v23
	v_cvt_pk_bf16_f32 v22, v26, v27
	v_cvt_pk_bf16_f32 v23, v24, v25
	ds_write_b128 v17, v[20:23] offset:64
	v_add_u32_e32 v20, 16, v18
	v_ashrrev_i32_e32 v21, 31, v20
	v_lshlrev_b64 v[20:21], 12, v[20:21]
	v_lshl_add_u64 v[28:29], s[18:19], 0, v[20:21]
	ds_read_b128 v[20:23], v30
	ds_read_b128 v[24:27], v30 offset:64
	v_lshl_add_u64 v[28:29], v[28:29], 0, s[4:5]
	v_lshl_add_u64 v[28:29], v[28:29], 0, s[34:35]
	v_lshl_add_u64 v[28:29], v[28:29], 0, v[178:179]
	s_waitcnt lgkmcnt(0)
	global_store_dwordx4 v[28:29], v[20:23], off sc1
	global_store_dwordx4 v[28:29], v[24:27], off offset:256 sc1
	s_nop 0
	v_pk_mul_f32 v[22:23], v[98:99], s[30:31] op_sel_hi:[1,0]
	v_pk_mul_f32 v[20:21], v[96:97], s[30:31] op_sel_hi:[1,0]
	v_pk_mul_f32 v[24:25], v[102:103], s[30:31] op_sel_hi:[1,0]
	v_pk_mul_f32 v[26:27], v[100:101], s[30:31] op_sel_hi:[1,0]
	v_cvt_pk_bf16_f32 v20, v20, v21
	v_cvt_pk_bf16_f32 v21, v22, v23
	v_cvt_pk_bf16_f32 v22, v26, v27
	v_cvt_pk_bf16_f32 v23, v24, v25
	ds_write_b128 v17, v[20:23]
	v_pk_mul_f32 v[22:23], v[134:135], s[30:31] op_sel_hi:[1,0]
	v_pk_mul_f32 v[20:21], v[132:133], s[30:31] op_sel_hi:[1,0]
	v_pk_mul_f32 v[24:25], v[138:139], s[30:31] op_sel_hi:[1,0]
	v_pk_mul_f32 v[26:27], v[136:137], s[30:31] op_sel_hi:[1,0]
	v_cvt_pk_bf16_f32 v20, v20, v21
	v_cvt_pk_bf16_f32 v21, v22, v23
	v_cvt_pk_bf16_f32 v22, v26, v27
	v_cvt_pk_bf16_f32 v23, v24, v25
	ds_write_b128 v17, v[20:23] offset:64
	v_add_u32_e32 v20, 32, v18
	v_ashrrev_i32_e32 v21, 31, v20
	v_lshlrev_b64 v[20:21], 12, v[20:21]
	v_lshl_add_u64 v[28:29], s[18:19], 0, v[20:21]
	ds_read_b128 v[20:23], v30
	ds_read_b128 v[24:27], v30 offset:64
	v_lshl_add_u64 v[28:29], v[28:29], 0, s[4:5]
	v_lshl_add_u64 v[28:29], v[28:29], 0, s[34:35]
	v_lshl_add_u64 v[28:29], v[28:29], 0, v[178:179]
	s_waitcnt lgkmcnt(0)
	global_store_dwordx4 v[28:29], v[20:23], off sc1
	global_store_dwordx4 v[28:29], v[24:27], off offset:256 sc1
	s_nop 0
	v_pk_mul_f32 v[22:23], v[82:83], s[30:31] op_sel_hi:[1,0]
	v_pk_mul_f32 v[20:21], v[80:81], s[30:31] op_sel_hi:[1,0]
	v_pk_mul_f32 v[24:25], v[86:87], s[30:31] op_sel_hi:[1,0]
	v_pk_mul_f32 v[26:27], v[84:85], s[30:31] op_sel_hi:[1,0]
	v_cvt_pk_bf16_f32 v20, v20, v21
	v_cvt_pk_bf16_f32 v21, v22, v23
	v_cvt_pk_bf16_f32 v22, v26, v27
	v_cvt_pk_bf16_f32 v23, v24, v25
	ds_write_b128 v17, v[20:23]
	v_pk_mul_f32 v[22:23], v[106:107], s[30:31] op_sel_hi:[1,0]
	v_pk_mul_f32 v[20:21], v[104:105], s[30:31] op_sel_hi:[1,0]
	v_pk_mul_f32 v[24:25], v[110:111], s[30:31] op_sel_hi:[1,0]
	v_pk_mul_f32 v[26:27], v[108:109], s[30:31] op_sel_hi:[1,0]
	v_cvt_pk_bf16_f32 v20, v20, v21
	v_cvt_pk_bf16_f32 v21, v22, v23
	v_cvt_pk_bf16_f32 v22, v26, v27
	v_cvt_pk_bf16_f32 v23, v24, v25
	ds_write_b128 v17, v[20:23] offset:64
	v_add_u32_e32 v20, 48, v18
	v_ashrrev_i32_e32 v21, 31, v20
	v_lshlrev_b64 v[20:21], 12, v[20:21]
	v_lshl_add_u64 v[28:29], s[18:19], 0, v[20:21]
	ds_read_b128 v[20:23], v30
	ds_read_b128 v[24:27], v30 offset:64
	v_lshl_add_u64 v[28:29], v[28:29], 0, s[4:5]
	v_lshl_add_u64 v[28:29], v[28:29], 0, s[34:35]
	v_lshl_add_u64 v[28:29], v[28:29], 0, v[178:179]
	s_waitcnt lgkmcnt(0)
	global_store_dwordx4 v[28:29], v[20:23], off sc1
	global_store_dwordx4 v[28:29], v[24:27], off offset:256 sc1
	s_nop 0
	v_pk_mul_f32 v[22:23], v[114:115], s[30:31] op_sel_hi:[1,0]
	v_pk_mul_f32 v[20:21], v[112:113], s[30:31] op_sel_hi:[1,0]
	v_pk_mul_f32 v[26:27], v[118:119], s[30:31] op_sel_hi:[1,0]
	v_pk_mul_f32 v[28:29], v[116:117], s[30:31] op_sel_hi:[1,0]
	v_cvt_pk_bf16_f32 v20, v20, v21
	v_cvt_pk_bf16_f32 v21, v22, v23
	v_cvt_pk_bf16_f32 v22, v28, v29
	v_cvt_pk_bf16_f32 v23, v26, v27
	v_add_u32_e32 v24, 0x80, v18
	ds_write_b128 v17, v[20:23]
	v_pk_mul_f32 v[22:23], v[154:155], s[30:31] op_sel_hi:[1,0]
	v_pk_mul_f32 v[20:21], v[152:153], s[30:31] op_sel_hi:[1,0]
	v_pk_mul_f32 v[26:27], v[158:159], s[30:31] op_sel_hi:[1,0]
	v_pk_mul_f32 v[28:29], v[156:157], s[30:31] op_sel_hi:[1,0]
	v_cvt_pk_bf16_f32 v20, v20, v21
	v_cvt_pk_bf16_f32 v21, v22, v23
	v_cvt_pk_bf16_f32 v22, v28, v29
	v_cvt_pk_bf16_f32 v23, v26, v27
	v_ashrrev_i32_e32 v25, 31, v24
	ds_write_b128 v17, v[20:23] offset:64
	v_lshlrev_b64 v[20:21], 12, v[24:25]
	v_lshl_add_u64 v[28:29], s[18:19], 0, v[20:21]
	ds_read_b128 v[20:23], v30
	ds_read_b128 v[24:27], v30 offset:64
	v_lshl_add_u64 v[28:29], v[28:29], 0, s[4:5]
	v_lshl_add_u64 v[28:29], v[28:29], 0, s[34:35]
	v_lshl_add_u64 v[28:29], v[28:29], 0, v[178:179]
	s_waitcnt lgkmcnt(0)
	global_store_dwordx4 v[28:29], v[20:23], off sc1
	global_store_dwordx4 v[28:29], v[24:27], off offset:256 sc1
	s_nop 0
	v_pk_mul_f32 v[22:23], v[90:91], s[30:31] op_sel_hi:[1,0]
	v_pk_mul_f32 v[20:21], v[88:89], s[30:31] op_sel_hi:[1,0]
	v_pk_mul_f32 v[24:25], v[94:95], s[30:31] op_sel_hi:[1,0]
	v_pk_mul_f32 v[26:27], v[92:93], s[30:31] op_sel_hi:[1,0]
	v_cvt_pk_bf16_f32 v20, v20, v21
	v_cvt_pk_bf16_f32 v21, v22, v23
	v_cvt_pk_bf16_f32 v22, v26, v27
	v_cvt_pk_bf16_f32 v23, v24, v25
	ds_write_b128 v17, v[20:23]
	v_pk_mul_f32 v[22:23], v[58:59], s[30:31] op_sel_hi:[1,0]
	v_pk_mul_f32 v[20:21], v[56:57], s[30:31] op_sel_hi:[1,0]
	v_pk_mul_f32 v[24:25], v[62:63], s[30:31] op_sel_hi:[1,0]
	v_pk_mul_f32 v[26:27], v[60:61], s[30:31] op_sel_hi:[1,0]
	v_cvt_pk_bf16_f32 v20, v20, v21
	v_cvt_pk_bf16_f32 v21, v22, v23
	v_cvt_pk_bf16_f32 v22, v26, v27
	v_cvt_pk_bf16_f32 v23, v24, v25
	ds_write_b128 v17, v[20:23] offset:64
	v_add_u32_e32 v20, 0x90, v18
	v_ashrrev_i32_e32 v21, 31, v20
	v_lshlrev_b64 v[20:21], 12, v[20:21]
	v_lshl_add_u64 v[28:29], s[18:19], 0, v[20:21]
	ds_read_b128 v[20:23], v30
	ds_read_b128 v[24:27], v30 offset:64
	v_lshl_add_u64 v[28:29], v[28:29], 0, s[4:5]
	v_lshl_add_u64 v[28:29], v[28:29], 0, s[34:35]
	v_pk_mul_f32 v[10:11], v[10:11], s[30:31] op_sel_hi:[1,0]
	v_pk_mul_f32 v[8:9], v[8:9], s[30:31] op_sel_hi:[1,0]
	v_pk_mul_f32 v[14:15], v[14:15], s[30:31] op_sel_hi:[1,0]
	v_pk_mul_f32 v[12:13], v[12:13], s[30:31] op_sel_hi:[1,0]
	v_lshl_add_u64 v[28:29], v[28:29], 0, v[178:179]
	v_cvt_pk_bf16_f32 v8, v8, v9
	v_cvt_pk_bf16_f32 v9, v10, v11
	v_cvt_pk_bf16_f32 v10, v12, v13
	v_cvt_pk_bf16_f32 v11, v14, v15
	s_waitcnt lgkmcnt(0)
	global_store_dwordx4 v[28:29], v[20:23], off sc1
	global_store_dwordx4 v[28:29], v[24:27], off offset:256 sc1
	ds_write_b128 v17, v[8:11] offset:64
	v_pk_mul_f32 v[22:23], v[74:75], s[30:31] op_sel_hi:[1,0]
	v_pk_mul_f32 v[20:21], v[72:73], s[30:31] op_sel_hi:[1,0]
	v_pk_mul_f32 v[24:25], v[78:79], s[30:31] op_sel_hi:[1,0]
	v_pk_mul_f32 v[26:27], v[76:77], s[30:31] op_sel_hi:[1,0]
	v_add_u32_e32 v8, 0xa0, v18
	v_cvt_pk_bf16_f32 v20, v20, v21
	v_cvt_pk_bf16_f32 v21, v22, v23
	v_cvt_pk_bf16_f32 v22, v26, v27
	v_cvt_pk_bf16_f32 v23, v24, v25
	v_ashrrev_i32_e32 v9, 31, v8
	ds_write_b128 v17, v[20:23]
	v_lshlrev_b64 v[8:9], 12, v[8:9]
	v_lshl_add_u64 v[20:21], s[18:19], 0, v[8:9]
	ds_read_b128 v[8:11], v30
	ds_read_b128 v[12:15], v30 offset:64
	v_lshl_add_u64 v[20:21], v[20:21], 0, s[4:5]
	v_lshl_add_u64 v[20:21], v[20:21], 0, s[34:35]
	v_lshl_add_u64 v[20:21], v[20:21], 0, v[178:179]
	s_waitcnt lgkmcnt(0)
	global_store_dwordx4 v[20:21], v[8:11], off sc1
	global_store_dwordx4 v[20:21], v[12:15], off offset:256 sc1
	s_nop 0
	v_pk_mul_f32 v[10:11], v[70:71], s[30:31] op_sel_hi:[1,0]
	v_pk_mul_f32 v[8:9], v[68:69], s[30:31] op_sel_hi:[1,0]
	v_pk_mul_f32 v[12:13], v[66:67], s[30:31] op_sel_hi:[1,0]
	v_pk_mul_f32 v[14:15], v[64:65], s[30:31] op_sel_hi:[1,0]
	v_cvt_pk_bf16_f32 v8, v8, v9
	v_cvt_pk_bf16_f32 v9, v10, v11
	v_cvt_pk_bf16_f32 v10, v14, v15
	v_cvt_pk_bf16_f32 v11, v12, v13
	ds_write_b128 v17, v[8:11]
	v_pk_mul_f32 v[6:7], v[6:7], s[30:31] op_sel_hi:[1,0]
	v_pk_mul_f32 v[4:5], v[4:5], s[30:31] op_sel_hi:[1,0]
	v_pk_mul_f32 v[8:9], v[2:3], s[30:31] op_sel_hi:[1,0]
	v_pk_mul_f32 v[2:3], v[0:1], s[30:31] op_sel_hi:[1,0]
	v_cvt_pk_bf16_f32 v0, v4, v5
	v_cvt_pk_bf16_f32 v1, v6, v7
	v_cvt_pk_bf16_f32 v2, v2, v3
	v_cvt_pk_bf16_f32 v3, v8, v9
	ds_write_b128 v17, v[0:3] offset:64
	v_add_u32_e32 v0, 0xb0, v18
	v_ashrrev_i32_e32 v1, 31, v0
	v_lshlrev_b64 v[0:1], 12, v[0:1]
	v_lshl_add_u64 v[8:9], s[18:19], 0, v[0:1]
	ds_read_b128 v[0:3], v30
	ds_read_b128 v[4:7], v30 offset:64
	v_lshl_add_u64 v[8:9], v[8:9], 0, s[4:5]
	v_lshl_add_u64 v[8:9], v[8:9], 0, s[34:35]
	v_lshl_add_u64 v[8:9], v[8:9], 0, v[178:179]
	s_mov_b64 s[4:5], -1
	s_andn2_b64 vcc, exec, s[2:3]
	s_mov_b32 s35, s36
	s_mov_b32 s44, s38
	s_mov_b64 s[46:47], s[42:43]
	s_mov_b64 s[48:49], s[40:41]
	s_waitcnt lgkmcnt(0)
	global_store_dwordx4 v[8:9], v[0:3], off sc1
	global_store_dwordx4 v[8:9], v[4:7], off offset:256 sc1
	s_cbranch_vccz .LBB0_2410
